# MLA full-tile loop: row sum with packed adds (18 instructions instead of 33)
# baseline (speedup 1.0000x reference)
.LBB0_695:
	v_pk_add_f32 v[4:5], v[66:67], v[68:69]
	v_pk_add_f32 v[6:7], v[70:71], v[72:73]
	v_pk_add_f32 v[4:5], v[4:5], v[74:75]
	v_pk_add_f32 v[6:7], v[6:7], v[76:77]
	v_pk_add_f32 v[4:5], v[4:5], v[78:79]
	v_pk_add_f32 v[6:7], v[6:7], v[82:83]
	v_pk_add_f32 v[4:5], v[4:5], v[84:85]
	v_pk_add_f32 v[6:7], v[6:7], v[86:87]
	v_pk_add_f32 v[4:5], v[4:5], v[88:89]
	v_pk_add_f32 v[6:7], v[6:7], v[90:91]
	v_pk_add_f32 v[4:5], v[4:5], v[92:93]
	v_pk_add_f32 v[6:7], v[6:7], v[94:95]
	v_pk_add_f32 v[4:5], v[4:5], v[208:209]
	v_pk_add_f32 v[4:5], v[4:5], v[6:7]
	v_add_f32_e32 v2, v96, v2
	s_add_i32 s10, s60, 1
	s_and_b32 s60, s10, 3
	s_waitcnt vmcnt(6) lgkmcnt(0)
	s_barrier
	s_add_i32 s10, s64, 1
	s_and_b32 s64, s10, 3
	s_add_i32 s73, s73, 1
	v_add_f32_e32 v4, v4, v5
	v_add_f32_e32 v2, v4, v2
	v_add_f32_e32 v191, v191, v2
	s_cmp_eq_u32 s71, s73
	s_cbranch_scc1 .LBB0_741
